# MoE phase: tile order permuted so that an XCD owns a contiguous range of slot tiles with all 8 column tiles each (A rows shared in one L2, expert weights read by about one XCD)
# speedup vs baseline: 1.0104x; 1.0104x over previous
; #define LAS __attribute__((address_space(3)))
; __global__ void __launch_bounds__(NTHR, 2) mk_fwd(Params prm) {
;     ...
;             case 7: { moe_offsets(c, layer, smi);
;                       const int n1v = (__builtin_amdgcn_readfirstlane(((const LAS int*)smi)[32]) >> 7) * 8;
;                       for (int t = bid; t < 2 * n1v; t += G) { asm volatile("" : "+v"(c.tid)); asm volatile("" : "+s"(c.p)); if (t < n1v) ph_moe1_mfma(c, layer, t, smi, smem_raw); else ph_moe2_mfma(c, layer, t - n1v, smi, smem_raw); } } break;
.LBB0_136:
	v_readlane_b32 s59, v254, 1
	s_nop 1
	s_mov_b32 s58, s59
	s_add_i32 s59, s59, s3
	s_add_i32 s58, s58, s3
	s_cmp_ge_i32 s59, s56
	s_cbranch_scc1 .LBB0_173
.LBB0_137:
	v_writelane_b32 v254, s59, 1
	s_lshr_b32 s16, s55, 3
	s_cmp_ge_i32 s59, s55
	s_cselect_b32 s6, s55, 0
	s_sub_i32 s7, s59, s6
	s_and_b32 s15, s7, 7
	s_lshr_b32 s7, s7, 3
	s_mul_i32 s15, s15, s16
	s_add_i32 s7, s7, s15
	s_add_i32 s59, s7, s6
	s_mov_b32 s58, s59
	ds_read_b32 v2, v3 offset:36032
	s_cmp_ge_i32 s59, s55
	s_mov_b64 s[6:7], -1
	s_waitcnt lgkmcnt(0)
	v_readfirstlane_b32 s15, v2
	s_cbranch_scc0 .LBB0_154
	s_sub_i32 s6, s59, s55
	s_lshr_b32 s16, s6, 3
	s_lshl_b32 s72, s16, 7
	s_cmp_ge_i32 s72, s15
	s_cbranch_scc1 .LBB0_153
	s_mov_b64 s[6:7], 0
	s_mov_b64 s[28:29], exec
	v_readlane_b32 s18, v253, 17
	v_readlane_b32 s19, v253, 18
	s_and_b64 s[18:19], s[28:29], s[18:19]
	s_mov_b64 exec, s[18:19]
	s_cbranch_execz .LBB0_141
	ds_read_b32 v2, v1 offset:35904
	s_waitcnt lgkmcnt(0)
	v_cmp_ge_i32_e32 vcc, s72, v2
	s_and_b64 s[6:7], vcc, exec
